# phase 1: counted vmcnt waits per k-step so the fp8 MFMAs start as each pair of A fragments lands
# baseline (speedup 1.0000x reference)
_Z7na_mainPKDF16_PKhS0_PKfS4_S4_S4_Pf:
	s_lshl_b32 s3, s2, 5
	s_and_b32 s3, s3, 0xe0
	s_ashr_i32 s2, s2, 3
	s_add_i32 s3, s3, s2
	s_ashr_i32 s2, s3, 6
	s_lshl_b32 s3, s3, 5
	s_and_b32 s14, s3, 0x7e0
	v_mov_b32_e32 v1, 0x7c0
	s_load_dwordx8 s[4:11], s[0:1], 0x0
	s_load_dwordx2 s[18:19], s[0:1], 0x20
	v_med3_u32 v1, s14, 32, v1
	v_subrev_u32_e32 v97, 32, v1
	s_ashr_i32 s3, s2, 31
	v_lshlrev_b32_e32 v58, 1, v97
	s_lshl_b64 s[12:13], s[2:3], 12
	v_mov_b32_e32 v59, 0
	v_sub_u32_e32 v60, s14, v97
	v_lshl_add_u64 v[10:11], s[12:13], 0, v[58:59]
	v_lshlrev_b64 v[2:3], 9, v[10:11]
	v_lshl_or_b32 v22, v60, 6, v0
	s_waitcnt lgkmcnt(0)
	v_and_b32_e32 v208, 31, v0
	v_lshlrev_b32_e32 v208, 5, v208
	global_load_dwordx4 v[192:195], v208, s[18:19]
	global_load_dwordx4 v[196:199], v208, s[18:19] offset:16
	v_lshl_add_u64 v[20:21], s[4:5], 0, v[2:3]
	v_ashrrev_i32_e32 v23, 31, v22
	v_lshl_add_u64 v[2:3], v[22:23], 4, v[20:21]
	global_load_dwordx4 v[12:15], v[2:3], off
	v_or_b32_e32 v28, 0x200, v22
	v_ashrrev_i32_e32 v29, 31, v28
	v_lshl_add_u64 v[2:3], v[28:29], 4, v[20:21]
	global_load_dwordx4 v[16:19], v[2:3], off
	v_or_b32_e32 v184, 0x400, v22
	v_ashrrev_i32_e32 v185, 31, v184
	v_lshl_add_u64 v[184:185], v[184:185], 4, v[20:21]
	v_or_b32_e32 v188, 0x600, v22
	v_ashrrev_i32_e32 v189, 31, v188
	v_lshl_add_u64 v[188:189], v[188:189], 4, v[20:21]
	global_load_dwordx4 v[184:187], v[184:185], off
	global_load_dwordx4 v[188:191], v[188:189], off
	v_lshrrev_b32_e32 v99, 6, v0
	v_and_b32_e32 v98, 63, v0
	v_lshlrev_b32_e32 v118, 13, v99
	v_lshl_or_b32 v58, v98, 5, v118
	s_movk_i32 s15, 0x1000
	v_lshl_add_u64 v[24:25], s[6:7], 0, v[58:59]
	v_or_b32_e32 v32, 0x400, v22
	v_or_b32_e32 v62, 0x600, v22
	v_add_co_u32_e32 v64, vcc, s15, v24
	s_mov_b64 s[12:13], 0x1000
	s_mov_b64 s[16:17], 0x1800
	v_lshlrev_b32_e32 v72, 1, v60
	v_lshrrev_b32_e32 v23, 5, v22
	v_and_b32_e32 v34, 32, v22
	v_ashrrev_i32_e32 v33, 31, v32
	v_ashrrev_i32_e32 v63, 31, v62
	v_addc_co_u32_e32 v65, vcc, 0, v25, vcc
	global_load_dwordx4 v[6:9], v58, s[6:7] offset:16
	global_load_dwordx4 v[2:5], v58, s[6:7]
	global_load_dwordx4 v[54:57], v58, s[6:7] offset:2064
	global_load_dwordx4 v[50:53], v58, s[6:7] offset:2048
	v_lshrrev_b32_e32 v58, 6, v22
	v_bfe_u32 v73, v22, 8, 2
	v_lshl_add_u64 v[26:27], v[24:25], 0, s[12:13]
	v_lshl_add_u64 v[24:25], v[24:25], 0, s[16:17]
	v_cmp_ne_u32_e32 vcc, 0, v34
	v_sub_u32_e32 v75, v23, v72
	global_load_dwordx4 v[42:45], v[64:65], off
	global_load_dwordx4 v[46:49], v[26:27], off offset:16
	global_load_dwordx4 v[34:37], v[64:65], off offset:2048
	global_load_dwordx4 v[38:41], v[24:25], off offset:16
	v_mov_b32_e32 v61, 0x60
	v_cndmask_b32_e32 v74, 0, v61, vcc
	v_add_u32_e32 v33, v74, v58
	v_lshlrev_b32_e32 v64, 2, v33
	v_bfe_u32 v96, v0, 4, 1
	v_and_b32_e32 v100, 15, v0
	v_mov_b32_e32 v30, v59
	v_mov_b32_e32 v31, v59
	v_and_b32_e32 v64, 12, v64
	v_mul_u32_u24_e32 v29, 0xc000, v96
	v_bitop3_b32 v64, v64, v100, v73 bitop3:0x36
	v_lshl_or_b32 v64, v64, 4, v29
	v_lshlrev_b32_e32 v63, 1, v75
	v_lshl_add_u32 v33, v33, 8, v64
	v_bfe_u32 v71, v0, 1, 4
	v_and_b32_e32 v70, 32, v0
	v_lshlrev_b32_e32 v1, 3, v0
	v_lshrrev_b32_e32 v58, 1, v75
	v_and_b32_e32 v1, 8, v1
	v_add_lshl_u32 v58, v58, v70, 8
	v_lshlrev_b32_e32 v121, 3, v99
	v_bfe_u32 v101, v0, 4, 2
	v_lshlrev_b32_e32 v102, 2, v101
	v_and_b32_e32 v116, 31, v0
	v_bfe_u32 v119, v0, 5, 1
	v_lshlrev_b32_e32 v124, 1, v119
	v_lshlrev_b32_e32 v117, 8, v116
	v_lshrrev_b32_e32 v95, 4, v0
	s_movk_i32 s16, 0x60
	s_mov_b32 s17, 0xc000
	v_and_b32_e32 v211, 3, v99
	v_lshrrev_b32_e32 v212, 2, v99
	v_lshl_or_b32 v211, v211, 2, v212
	v_xor_b32_e32 v213, v100, v211
	v_mul_u32_u24_e32 v214, 0x60, v119
	v_add3_u32 v214, v214, v60, v99
	v_mul_u32_u24_e32 v215, 0xc000, v96
	v_lshl_add_u32 v214, v214, 8, v215
	v_lshl_or_b32 v220, v213, 4, v214
	v_xor_b32_e32 v221, 32, v220
	v_xor_b32_e32 v216, v71, v211
	v_lshl_add_u32 v217, v119, 5, v99
	v_lshlrev_b32_e32 v217, 8, v217
	v_lshl_or_b32 v216, v216, 4, v217
	v_or_b32_e32 v216, v216, v1
	v_add_u32_e32 v222, 0x23800, v216
	v_xor_b32_e32 v223, 32, v222
	s_waitcnt vmcnt(11)
	ds_write_b128 v220, v[12:15]
	v_fma_mix_f32 v200, v192, v12, 0 op_sel_hi:[0,1,0]
	v_fma_mix_f32 v201, v193, v12, 0 op_sel:[0,1,0] op_sel_hi:[0,1,0]
	v_cvt_f32_f16_e32 v211, v12
	v_cvt_f32_f16_sdwa v212, v12 dst_sel:DWORD dst_unused:UNUSED_PAD src0_sel:WORD_1
	v_fma_mix_f32 v200, v194, v13, v200 op_sel_hi:[0,1,0]
	v_fma_mix_f32 v201, v195, v13, v201 op_sel:[0,1,0] op_sel_hi:[0,1,0]
	v_cvt_f32_f16_e32 v213, v13
	v_cvt_f32_f16_sdwa v214, v13 dst_sel:DWORD dst_unused:UNUSED_PAD src0_sel:WORD_1
	v_fma_mix_f32 v200, v196, v14, v200 op_sel_hi:[0,1,0]
	v_fma_mix_f32 v201, v197, v14, v201 op_sel:[0,1,0] op_sel_hi:[0,1,0]
	v_cvt_f32_f16_e32 v215, v14
	v_cvt_f32_f16_sdwa v216, v14 dst_sel:DWORD dst_unused:UNUSED_PAD src0_sel:WORD_1
	v_fma_mix_f32 v200, v198, v15, v200 op_sel_hi:[0,1,0]
	v_fma_mix_f32 v201, v199, v15, v201 op_sel:[0,1,0] op_sel_hi:[0,1,0]
	v_cvt_f32_f16_e32 v217, v15
	v_cvt_f32_f16_sdwa v218, v15 dst_sel:DWORD dst_unused:UNUSED_PAD src0_sel:WORD_1
	v_cvt_pk_fp8_f32 v224, v211, v212
	v_cvt_pk_fp8_f32 v225, v215, v216
	v_cvt_pk_fp8_f32 v224, v213, v214 op_sel:[0,0,1]
	v_cvt_pk_fp8_f32 v225, v217, v218 op_sel:[0,0,1]
	s_nop 0
	ds_write_b64 v222, v[224:225]
	s_waitcnt vmcnt(10)
	ds_write_b128 v221, v[16:19] offset:2048
	v_fma_mix_f32 v202, v192, v16, 0 op_sel_hi:[0,1,0]
	v_fma_mix_f32 v203, v193, v16, 0 op_sel:[0,1,0] op_sel_hi:[0,1,0]
	v_cvt_f32_f16_e32 v211, v16
	v_cvt_f32_f16_sdwa v212, v16 dst_sel:DWORD dst_unused:UNUSED_PAD src0_sel:WORD_1
	v_fma_mix_f32 v202, v194, v17, v202 op_sel_hi:[0,1,0]
	v_fma_mix_f32 v203, v195, v17, v203 op_sel:[0,1,0] op_sel_hi:[0,1,0]
	v_cvt_f32_f16_e32 v213, v17
	v_cvt_f32_f16_sdwa v214, v17 dst_sel:DWORD dst_unused:UNUSED_PAD src0_sel:WORD_1
	v_fma_mix_f32 v202, v196, v18, v202 op_sel_hi:[0,1,0]
	v_fma_mix_f32 v203, v197, v18, v203 op_sel:[0,1,0] op_sel_hi:[0,1,0]
	v_cvt_f32_f16_e32 v215, v18
	v_cvt_f32_f16_sdwa v216, v18 dst_sel:DWORD dst_unused:UNUSED_PAD src0_sel:WORD_1
	v_fma_mix_f32 v202, v198, v19, v202 op_sel_hi:[0,1,0]
	v_fma_mix_f32 v203, v199, v19, v203 op_sel:[0,1,0] op_sel_hi:[0,1,0]
	v_cvt_f32_f16_e32 v217, v19
	v_cvt_f32_f16_sdwa v218, v19 dst_sel:DWORD dst_unused:UNUSED_PAD src0_sel:WORD_1
	v_cvt_pk_fp8_f32 v226, v211, v212
	v_cvt_pk_fp8_f32 v227, v215, v216
	v_cvt_pk_fp8_f32 v226, v213, v214 op_sel:[0,0,1]
	v_cvt_pk_fp8_f32 v227, v217, v218 op_sel:[0,0,1]
	s_nop 0
	ds_write_b64 v223, v[226:227] offset:2048
	s_waitcnt vmcnt(9)
	ds_write_b128 v220, v[184:187] offset:4096
	v_fma_mix_f32 v204, v192, v184, 0 op_sel_hi:[0,1,0]
	v_fma_mix_f32 v205, v193, v184, 0 op_sel:[0,1,0] op_sel_hi:[0,1,0]
	v_cvt_f32_f16_e32 v211, v184
	v_cvt_f32_f16_sdwa v212, v184 dst_sel:DWORD dst_unused:UNUSED_PAD src0_sel:WORD_1
	v_fma_mix_f32 v204, v194, v185, v204 op_sel_hi:[0,1,0]
	v_fma_mix_f32 v205, v195, v185, v205 op_sel:[0,1,0] op_sel_hi:[0,1,0]
	v_cvt_f32_f16_e32 v213, v185
	v_cvt_f32_f16_sdwa v214, v185 dst_sel:DWORD dst_unused:UNUSED_PAD src0_sel:WORD_1
	v_fma_mix_f32 v204, v196, v186, v204 op_sel_hi:[0,1,0]
	v_fma_mix_f32 v205, v197, v186, v205 op_sel:[0,1,0] op_sel_hi:[0,1,0]
	v_cvt_f32_f16_e32 v215, v186
	v_cvt_f32_f16_sdwa v216, v186 dst_sel:DWORD dst_unused:UNUSED_PAD src0_sel:WORD_1
	v_fma_mix_f32 v204, v198, v187, v204 op_sel_hi:[0,1,0]
	v_fma_mix_f32 v205, v199, v187, v205 op_sel:[0,1,0] op_sel_hi:[0,1,0]
	v_cvt_f32_f16_e32 v217, v187
	v_cvt_f32_f16_sdwa v218, v187 dst_sel:DWORD dst_unused:UNUSED_PAD src0_sel:WORD_1
	v_cvt_pk_fp8_f32 v228, v211, v212
	v_cvt_pk_fp8_f32 v229, v215, v216
	v_cvt_pk_fp8_f32 v228, v213, v214 op_sel:[0,0,1]
	v_cvt_pk_fp8_f32 v229, v217, v218 op_sel:[0,0,1]
	s_nop 0
	ds_write_b64 v222, v[228:229] offset:4096
	s_waitcnt vmcnt(8)
	ds_write_b128 v221, v[188:191] offset:6144
	v_fma_mix_f32 v206, v192, v188, 0 op_sel_hi:[0,1,0]
	v_fma_mix_f32 v207, v193, v188, 0 op_sel:[0,1,0] op_sel_hi:[0,1,0]
	v_cvt_f32_f16_e32 v211, v188
	v_cvt_f32_f16_sdwa v212, v188 dst_sel:DWORD dst_unused:UNUSED_PAD src0_sel:WORD_1
	v_fma_mix_f32 v206, v194, v189, v206 op_sel_hi:[0,1,0]
	v_fma_mix_f32 v207, v195, v189, v207 op_sel:[0,1,0] op_sel_hi:[0,1,0]
	v_cvt_f32_f16_e32 v213, v189
	v_cvt_f32_f16_sdwa v214, v189 dst_sel:DWORD dst_unused:UNUSED_PAD src0_sel:WORD_1
	v_fma_mix_f32 v206, v196, v190, v206 op_sel_hi:[0,1,0]
	v_fma_mix_f32 v207, v197, v190, v207 op_sel:[0,1,0] op_sel_hi:[0,1,0]
	v_cvt_f32_f16_e32 v215, v190
	v_cvt_f32_f16_sdwa v216, v190 dst_sel:DWORD dst_unused:UNUSED_PAD src0_sel:WORD_1
	v_fma_mix_f32 v206, v198, v191, v206 op_sel_hi:[0,1,0]
	v_fma_mix_f32 v207, v199, v191, v207 op_sel:[0,1,0] op_sel_hi:[0,1,0]
	v_cvt_f32_f16_e32 v217, v191
	v_cvt_f32_f16_sdwa v218, v191 dst_sel:DWORD dst_unused:UNUSED_PAD src0_sel:WORD_1
	v_cvt_pk_fp8_f32 v230, v211, v212
	v_cvt_pk_fp8_f32 v231, v215, v216
	v_cvt_pk_fp8_f32 v230, v213, v214 op_sel:[0,0,1]
	v_cvt_pk_fp8_f32 v231, v217, v218 op_sel:[0,0,1]
	s_nop 0
	ds_write_b64 v223, v[230:231] offset:6144
	v_add_f32_e32 v200, v200, v201
	v_add_f32_e32 v202, v202, v203
	v_add_f32_e32 v204, v204, v205
	v_add_f32_e32 v206, v206, v207
	v_lshlrev_b32_e32 v208, 7, v119
	v_lshl_add_u32 v208, v99, 2, v208
	v_add_u32_e32 v208, 0x27800, v208
	v_add_f32_dpp v200, v200, v200 quad_perm:[1,0,3,2] row_mask:0xf bank_mask:0xf
	v_add_f32_dpp v202, v202, v202 quad_perm:[1,0,3,2] row_mask:0xf bank_mask:0xf
	v_add_f32_dpp v204, v204, v204 quad_perm:[1,0,3,2] row_mask:0xf bank_mask:0xf
	v_add_f32_dpp v206, v206, v206 quad_perm:[1,0,3,2] row_mask:0xf bank_mask:0xf
	v_add_f32_dpp v200, v200, v200 quad_perm:[2,3,0,1] row_mask:0xf bank_mask:0xf
	v_add_f32_dpp v202, v202, v202 quad_perm:[2,3,0,1] row_mask:0xf bank_mask:0xf
	v_add_f32_dpp v204, v204, v204 quad_perm:[2,3,0,1] row_mask:0xf bank_mask:0xf
	v_add_f32_dpp v206, v206, v206 quad_perm:[2,3,0,1] row_mask:0xf bank_mask:0xf
	v_add_f32_dpp v200, v200, v200 row_half_mirror row_mask:0xf bank_mask:0xf
	v_add_f32_dpp v202, v202, v202 row_half_mirror row_mask:0xf bank_mask:0xf
	v_add_f32_dpp v204, v204, v204 row_half_mirror row_mask:0xf bank_mask:0xf
	v_add_f32_dpp v206, v206, v206 row_half_mirror row_mask:0xf bank_mask:0xf
	v_add_f32_dpp v200, v200, v200 row_mirror row_mask:0xf bank_mask:0xf
	v_add_f32_dpp v202, v202, v202 row_mirror row_mask:0xf bank_mask:0xf
	v_add_f32_dpp v204, v204, v204 row_mirror row_mask:0xf bank_mask:0xf
	v_add_f32_dpp v206, v206, v206 row_mirror row_mask:0xf bank_mask:0xf
	v_add_f32_dpp v200, v200, v200 row_bcast:15 row_mask:0xa bank_mask:0xf
	v_add_f32_dpp v202, v202, v202 row_bcast:15 row_mask:0xa bank_mask:0xf
	v_add_f32_dpp v204, v204, v204 row_bcast:15 row_mask:0xa bank_mask:0xf
	v_add_f32_dpp v206, v206, v206 row_bcast:15 row_mask:0xa bank_mask:0xf
	s_mov_b32 exec_lo, 0xffff0000
	s_mov_b32 exec_hi, 0xffff0000
	ds_write_b32 v208, v200
	ds_write_b32 v208, v202 offset:32
	ds_write_b32 v208, v204 offset:64
	ds_write_b32 v208, v206 offset:96
	s_mov_b64 exec, -1
	v_cmp_lt_i32_e32 vcc, v121, v60
	s_nop 0
	v_mov_b32_e32 v15, v59
	v_cndmask_b32_e64 v12, 32, 0, vcc
	v_add_u32_e32 v16, v12, v121
	v_or_b32_e32 v12, v16, v101
	v_lshlrev_b32_e32 v58, 1, v12
	v_lshrrev_b32_e32 v12, 5, v0
	v_and_b32_e32 v12, 2, v12
	v_bitop3_b32 v14, v102, v100, v12 bitop3:0x36
	v_lshl_add_u64 v[12:13], v[10:11], 0, v[58:59]
	v_lshlrev_b64 v[12:13], 9, v[12:13]
	v_lshlrev_b32_e32 v16, 8, v16
	v_lshl_add_u64 v[12:13], s[4:5], 0, v[12:13]
	v_lshlrev_b32_e32 v14, 4, v14
	v_readfirstlane_b32 s6, v16
	v_add_u32_e32 v17, 0xc000, v16
	v_lshl_add_u64 v[12:13], v[12:13], 0, v[14:15]
	s_mov_b32 m0, s6
	s_mov_b64 s[6:7], 0x100
	v_readfirstlane_b32 s12, v17
	global_load_lds_dwordx4 v[12:13], off
	v_lshl_add_u64 v[12:13], v[12:13], 0, s[6:7]
	s_mov_b32 m0, s12
	v_or_b32_e32 v58, 1, v58
	global_load_lds_dwordx4 v[12:13], off
	v_lshl_add_u64 v[12:13], v[10:11], 0, v[58:59]
	v_lshlrev_b64 v[12:13], 9, v[12:13]
	v_lshl_add_u64 v[12:13], s[4:5], 0, v[12:13]
	v_lshl_add_u64 v[12:13], v[12:13], 0, v[14:15]
	v_add_u32_e32 v14, 0x6000, v16
	v_bfe_u32 v61, v0, 2, 2
	v_readfirstlane_b32 s12, v14
	v_add_u32_e32 v14, 0x12000, v16
	s_mov_b32 m0, s12
	v_readfirstlane_b32 s12, v14
	global_load_lds_dwordx4 v[12:13], off
	v_lshl_add_u64 v[12:13], v[12:13], 0, s[6:7]
	s_mov_b32 m0, s12
	v_add_u32_e32 v18, 0x23800, v117
	global_load_lds_dwordx4 v[12:13], off
	v_or_b32_e32 v12, 4, v121
	v_cmp_lt_i32_e32 vcc, v12, v60
	s_nop 1
	v_cndmask_b32_e64 v13, 32, 0, vcc
	v_add_u32_e32 v16, v13, v12
	v_or_b32_e32 v13, v16, v101
	v_lshlrev_b32_e32 v58, 1, v13
	v_bfe_u32 v12, v12, 2, 2
	v_bitop3_b32 v14, v102, v100, v12 bitop3:0x36
	v_lshl_add_u64 v[12:13], v[10:11], 0, v[58:59]
	v_lshlrev_b64 v[12:13], 9, v[12:13]
	v_lshlrev_b32_e32 v16, 8, v16
	v_lshl_add_u64 v[12:13], s[4:5], 0, v[12:13]
	v_lshlrev_b32_e32 v14, 4, v14
	v_readfirstlane_b32 s12, v16
	v_add_u32_e32 v17, 0xc000, v16
	v_lshl_add_u64 v[12:13], v[12:13], 0, v[14:15]
	s_mov_b32 m0, s12
	v_readfirstlane_b32 s12, v17
	v_or_b32_e32 v58, 1, v58
	global_load_lds_dwordx4 v[12:13], off
	v_lshl_add_u64 v[12:13], v[12:13], 0, s[6:7]
	s_mov_b32 m0, s12
	v_lshl_add_u64 v[10:11], v[10:11], 0, v[58:59]
	global_load_lds_dwordx4 v[12:13], off
	v_lshlrev_b64 v[10:11], 9, v[10:11]
	v_add_u32_e32 v12, 0x6000, v16
	v_lshl_add_u64 v[10:11], s[4:5], 0, v[10:11]
	v_readfirstlane_b32 s4, v12
	v_add_u32_e32 v12, 0x12000, v16
	v_lshl_add_u64 v[10:11], v[10:11], 0, v[14:15]
	s_mov_b32 m0, s4
	v_readfirstlane_b32 s4, v12
	global_load_lds_dwordx4 v[10:11], off
	v_lshl_add_u64 v[10:11], v[10:11], 0, s[6:7]
	s_mov_b32 m0, s4
	s_nop 0
	global_load_lds_dwordx4 v[10:11], off
	s_waitcnt lgkmcnt(0)
	s_barrier
	v_lshlrev_b32_e32 v10, 2, v0
	v_and_b32_e32 v94, 12, v10
	v_or_b32_e32 v120, v94, v61
	v_bitop3_b32 v10, v124, v94, v61 bitop3:0x1e
	v_lshl_or_b32 v14, v10, 4, v18
	v_bitop3_b32 v10, v124, v120, 1 bitop3:0x36
	v_lshl_or_b32 v19, v10, 4, v18
	s_load_dwordx4 s[4:7], s[0:1], 0x20
	s_load_dwordx2 s[12:13], s[0:1], 0x38
	ds_read_b128 v[10:13], v14
	ds_read_b128 v[62:65], v14 offset:8192
	ds_read_b128 v[14:17], v19
	ds_read_b128 v[66:69], v19 offset:8192
	v_bitop3_b32 v19, v124, v120, 4 bitop3:0x36
	v_lshl_or_b32 v19, v19, 4, v18
	v_bitop3_b32 v20, v124, v120, 5 bitop3:0x36
	v_lshl_or_b32 v20, v20, 4, v18
	ds_read_b128 v[70:73], v19
	ds_read_b128 v[78:81], v19 offset:8192
	ds_read_b128 v[74:77], v20
	ds_read_b128 v[82:85], v20 offset:8192
	v_bitop3_b32 v19, v124, v120, 8 bitop3:0x36
	v_lshl_or_b32 v19, v19, 4, v18
	v_bitop3_b32 v20, v124, v120, 9 bitop3:0x36
	v_lshl_or_b32 v20, v20, 4, v18
	ds_read_b128 v[86:89], v19
	ds_read_b128 v[104:107], v19 offset:8192
	ds_read_b128 v[90:93], v20
	ds_read_b128 v[108:111], v20 offset:8192
	v_bitop3_b32 v19, v124, v120, 12 bitop3:0x36
	v_lshl_or_b32 v19, v19, 4, v18
	v_bitop3_b32 v20, v124, v120, 13 bitop3:0x36
	v_lshl_or_b32 v18, v20, 4, v18
	ds_read_b128 v[126:129], v19
	ds_read_b128 v[134:137], v19 offset:8192
	ds_read_b128 v[130:133], v18
	ds_read_b128 v[138:141], v18 offset:8192
	v_mov_b32_e32 v103, 0x7f
	v_lshlrev_b32_e32 v58, 7, v99
	v_or_b32_e32 v122, 0x18000, v117
	s_waitcnt vmcnt(14) lgkmcnt(0)
	v_mfma_scale_f32_32x32x64_f8f6f4 v[18:33], v[2:9], v[10:17], 0, v103, v103 op_sel_hi:[0,0,0]
	v_lshlrev_b32_e32 v125, 3, v119
	v_or_b32_e32 v123, 0x1a000, v117
	v_mfma_scale_f32_32x32x64_f8f6f4 v[2:17], v[2:9], v[62:69], 0, v103, v103 op_sel_hi:[0,0,0]
	v_and_b32_e32 v62, 12, v95
	s_waitcnt vmcnt(12)
	v_mfma_scale_f32_32x32x64_f8f6f4 v[18:33], v[50:57], v[70:77], v[18:33], v103, v103 op_sel_hi:[0,0,0]
	v_mfma_scale_f32_32x32x64_f8f6f4 v[2:17], v[50:57], v[78:85], v[2:17], v103, v103 op_sel_hi:[0,0,0]
	v_lshl_add_u64 v[50:51], s[10:11], 0, v[58:59]
	v_lshlrev_b32_e32 v58, 4, v119
	v_lshl_add_u64 v[54:55], v[50:51], 0, v[58:59]
	global_load_dwordx4 v[50:53], v[54:55], off
	s_brev_b32 s10, 60
	v_lshlrev_b32_e32 v58, 6, v0
	v_and_b32_e32 v58, 0x4000, v58
	v_or3_b32 v63, v122, v58, v125
	v_or3_b32 v58, v123, v58, v125
	s_waitcnt vmcnt(11)
	v_mfma_scale_f32_32x32x64_f8f6f4 v[18:33], v[42:49], v[86:93], v[18:33], v103, v103 op_sel_hi:[0,0,0]
	v_mfma_scale_f32_32x32x64_f8f6f4 v[2:17], v[42:49], v[104:111], v[2:17], v103, v103 op_sel_hi:[0,0,0]
	global_load_dwordx4 v[42:45], v[54:55], off offset:32
	global_load_dwordx4 v[46:49], v[54:55], off offset:64
	s_nop 0
	global_load_dwordx4 v[54:57], v[54:55], off offset:96
	s_waitcnt vmcnt(12)
	v_mfma_scale_f32_32x32x64_f8f6f4 v[2:17], v[34:41], v[134:141], v[2:17], v103, v103 op_sel_hi:[0,0,0]
	v_mfma_scale_f32_32x32x64_f8f6f4 v[18:33], v[34:41], v[126:133], v[18:33], v103, v103 op_sel_hi:[0,0,0]
	s_waitcnt vmcnt(0)
	s_nop 15
	s_nop 1
	v_fma_f32 v2, v2, s10, v50
	v_fma_f32 v3, v3, s10, v51
	v_fma_f32 v4, v4, s10, v52
	v_fma_f32 v5, v5, s10, v53
	v_cvt_pk_f16_f32 v2, v2, v3
	v_cvt_pk_f16_f32 v3, v4, v5
	v_bitop3_b32 v4, v95, v120, 12 bitop3:0x6c
	v_pk_fma_f32 v[18:19], v[18:19], s[10:11], v[50:51] op_sel_hi:[1,0,1]
	v_pk_fma_f32 v[20:21], v[20:21], s[10:11], v[52:53] op_sel_hi:[1,0,1]
	v_lshlrev_b32_e32 v4, 4, v4
	v_cvt_pk_f16_f32 v18, v18, v19
	v_cvt_pk_f16_f32 v19, v20, v21
	v_or_b32_e32 v5, v63, v4
	v_or_b32_e32 v4, v58, v4
	ds_write_b64 v5, v[18:19]
	ds_write_b64 v4, v[2:3]
	v_pk_fma_f32 v[2:3], v[22:23], s[10:11], v[42:43] op_sel_hi:[1,0,1]
	v_pk_fma_f32 v[4:5], v[6:7], s[10:11], v[42:43] op_sel_hi:[1,0,1]
	v_pk_fma_f32 v[6:7], v[24:25], s[10:11], v[44:45] op_sel_hi:[1,0,1]
	v_cvt_pk_f16_f32 v2, v2, v3
	v_cvt_pk_f16_f32 v3, v6, v7
	v_pk_fma_f32 v[6:7], v[8:9], s[10:11], v[44:45] op_sel_hi:[1,0,1]
	v_cvt_pk_f16_f32 v4, v4, v5
	v_cvt_pk_f16_f32 v5, v6, v7
	v_bitop3_b32 v6, v62, v120, 1 bitop3:0x36
	v_lshlrev_b32_e32 v6, 4, v6
	v_or_b32_e32 v7, v63, v6
	ds_write_b64 v7, v[2:3]
	v_or_b32_e32 v2, v58, v6
	ds_write_b64 v2, v[4:5]
	v_pk_fma_f32 v[2:3], v[26:27], s[10:11], v[46:47] op_sel_hi:[1,0,1]
	v_pk_fma_f32 v[6:7], v[28:29], s[10:11], v[48:49] op_sel_hi:[1,0,1]
	v_cvt_pk_f16_f32 v2, v2, v3
	v_pk_fma_f32 v[4:5], v[10:11], s[10:11], v[46:47] op_sel_hi:[1,0,1]
	v_cvt_pk_f16_f32 v3, v6, v7
	v_pk_fma_f32 v[6:7], v[12:13], s[10:11], v[48:49] op_sel_hi:[1,0,1]
	v_cvt_pk_f16_f32 v4, v4, v5
	v_cvt_pk_f16_f32 v5, v6, v7
	v_bitop3_b32 v6, v62, v120, 2 bitop3:0x36
	v_lshlrev_b32_e32 v6, 4, v6
	v_or_b32_e32 v7, v63, v6
	ds_write_b64 v7, v[2:3]
	v_or_b32_e32 v2, v58, v6
	ds_write_b64 v2, v[4:5]
	v_pk_fma_f32 v[2:3], v[30:31], s[10:11], v[54:55] op_sel_hi:[1,0,1]
	v_pk_fma_f32 v[6:7], v[32:33], s[10:11], v[56:57] op_sel_hi:[1,0,1]
	v_cvt_pk_f16_f32 v2, v2, v3
	v_pk_fma_f32 v[4:5], v[14:15], s[10:11], v[54:55] op_sel_hi:[1,0,1]
	v_cvt_pk_f16_f32 v3, v6, v7
	v_pk_fma_f32 v[6:7], v[16:17], s[10:11], v[56:57] op_sel_hi:[1,0,1]
	v_cvt_pk_f16_f32 v4, v4, v5
	v_cvt_pk_f16_f32 v5, v6, v7
	v_bitop3_b32 v6, v62, v120, 3 bitop3:0x36
	v_lshlrev_b32_e32 v6, 4, v6
	v_or_b32_e32 v7, v63, v6
	ds_write_b64 v7, v[2:3]
	v_or_b32_e32 v2, v58, v6
	ds_write_b64 v2, v[4:5]
	s_waitcnt lgkmcnt(0)
	s_barrier
	v_and_b32_e32 v236, 1, v101
	v_lshrrev_b32_e32 v237, 1, v101
	v_xor_b32_e32 v237, v237, v236
	v_lshl_or_b32 v236, v236, 1, v237
	v_lshrrev_b32_e32 v27, 8, v0
	v_lshrrev_b32_e32 v3, 3, v0
	v_and_b32_e32 v3, 16, v3
	v_mul_u32_u24_e32 v28, 0x60, v27
	v_lshlrev_b32_e32 v26, 5, v27
	v_or_b32_e32 v146, v3, v100
	v_or_b32_e32 v147, v28, v100
	v_or_b32_e32 v4, v146, v26
	v_lshlrev_b32_e32 v209, 2, v4
	v_add_u32_e32 v209, 0x27800, v209
	v_lshlrev_b32_e32 v4, 8, v4
	v_or_b32_e32 v5, 0x18000, v4
	v_bitop3_b32 v11, v236, v120, 12 bitop3:0x36
	v_or_b32_e32 v95, 0x1c000, v4
	v_lshlrev_b32_e32 v29, 3, v101
	v_bitop3_b32 v6, v236, v94, v61 bitop3:0x1e
	v_bitop3_b32 v8, v236, v120, 4 bitop3:0x36
	v_bitop3_b32 v10, v236, v120, 8 bitop3:0x36
	v_lshlrev_b32_e32 v94, 4, v11
	v_lshlrev_b32_e32 v6, 4, v6
	v_lshlrev_b32_e32 v8, 4, v8
	v_lshlrev_b32_e32 v58, 4, v10
	v_or_b32_e32 v7, v5, v6
	v_or_b32_e32 v9, v5, v8
	v_or_b32_e32 v10, v5, v58
	v_or_b32_e32 v5, v5, v94
	v_or_b32_e32 v6, v95, v6
	v_or_b32_e32 v60, v95, v8
	ds_read_b128 v[22:25], v7
	ds_read_b128 v[18:21], v9
	ds_read_b128 v[14:17], v10
	ds_read_b128 v[10:13], v5
	ds_read_b128 v[6:9], v6
	ds_read_b128 v[2:5], v60
	v_bfe_u32 v103, v0, 6, 1
	s_movk_i32 s5, 0x2000
	v_mad_u32_u24 v44, v103, 48, v147
	v_lshlrev_b32_e32 v60, 8, v44
	v_lshlrev_b32_e32 v44, 2, v44
	v_or_b32_e32 v35, v95, v58
	v_lshlrev_b32_e32 v58, 14, v99
	v_and_b32_e32 v44, 12, v44
	v_or_b32_e32 v56, v44, v61
	v_bitop3_b32 v44, v236, v44, v61 bitop3:0x1e
	v_lshl_add_u64 v[32:33], s[8:9], 0, v[58:59]
	v_lshlrev_b32_e32 v58, 4, v98
	v_or_b32_e32 v36, v95, v94
	v_lshl_add_u64 v[88:89], v[32:33], 0, v[58:59]
	v_lshl_or_b32 v57, v44, 4, v60
	ds_read_b128 v[40:43], v35
	ds_read_b128 v[106:109], v36
	s_load_dword s4, s[6:7], 0x0
	global_load_dwordx4 v[36:39], v[88:89], off
	global_load_dwordx4 v[32:35], v[88:89], off offset:1024
	ds_read_b128 v[44:47], v57
	v_bitop3_b32 v48, v236, v56, 4 bitop3:0x36
	v_lshl_or_b32 v62, v48, 4, v60
	ds_read_b128 v[48:51], v62
	v_bitop3_b32 v52, v236, v56, 8 bitop3:0x36
	v_lshl_or_b32 v63, v52, 4, v60
	ds_read_b128 v[52:55], v63
	s_waitcnt lgkmcnt(0)
	v_mfma_f32_16x16x32_f16 v[44:47], v[44:47], v[22:25], 0
	v_bitop3_b32 v64, v236, v56, 12 bitop3:0x36
	ds_read_b128 v[56:59], v57 offset:49152
	v_lshl_or_b32 v60, v64, 4, v60
	v_mfma_f32_16x16x32_f16 v[44:47], v[48:51], v[18:21], v[44:47]
	ds_read_b128 v[68:71], v60
	ds_read_b128 v[72:75], v62 offset:49152
	v_mad_u32_u24 v104, v103, 3, 1
	v_lshlrev_b32_e32 v132, 4, v104
	v_mfma_f32_16x16x32_f16 v[44:47], v[52:55], v[14:17], v[44:47]
	v_add_u32_e32 v52, v132, v147
	global_load_dwordx4 v[64:67], v[88:89], off offset:2048
	global_load_dwordx4 v[48:51], v[88:89], off offset:3072
	ds_read_b128 v[76:79], v63 offset:49152
	ds_read_b128 v[80:83], v60 offset:49152
	s_waitcnt lgkmcnt(3)
	v_mfma_f32_16x16x32_f16 v[44:47], v[68:71], v[10:13], v[44:47]
	v_lshlrev_b32_e32 v60, 8, v52
	v_lshlrev_b32_e32 v52, 2, v52
	v_and_b32_e32 v52, 12, v52
	v_mfma_f32_16x16x32_f16 v[44:47], v[56:59], v[6:9], v[44:47]
	v_or_b32_e32 v62, v52, v61
	v_bitop3_b32 v52, v236, v52, v61 bitop3:0x1e
	v_lshl_or_b32 v63, v52, 4, v60
	s_waitcnt lgkmcnt(2)
	v_mfma_f32_16x16x32_f16 v[44:47], v[72:75], v[2:5], v[44:47]
	ds_read_b128 v[52:55], v63
	v_bitop3_b32 v56, v236, v62, 4 bitop3:0x36
	v_lshl_or_b32 v84, v56, 4, v60
	s_waitcnt lgkmcnt(2)
	v_mfma_f32_16x16x32_f16 v[44:47], v[76:79], v[40:43], v[44:47]
	ds_read_b128 v[56:59], v84
	v_bitop3_b32 v68, v236, v62, 8 bitop3:0x36
	v_lshl_or_b32 v85, v68, 4, v60
	s_waitcnt lgkmcnt(2)
	v_mfma_f32_16x16x32_f16 v[110:113], v[80:83], v[106:109], v[44:47]
	ds_read_b128 v[68:71], v63 offset:49152
	v_bitop3_b32 v62, v236, v62, 12 bitop3:0x36
	v_lshl_or_b32 v60, v62, 4, v60
	ds_read_b128 v[44:47], v85
	s_waitcnt lgkmcnt(3)
	v_mfma_f32_16x16x32_f16 v[52:55], v[52:55], v[22:25], 0
	ds_read_b128 v[72:75], v60
	ds_read_b128 v[76:79], v84 offset:49152
	v_mad_u32_u24 v105, v103, 3, 2
	v_lshlrev_b32_e32 v133, 4, v105
	s_waitcnt lgkmcnt(4)
	v_mfma_f32_16x16x32_f16 v[52:55], v[56:59], v[18:21], v[52:55]
	ds_read_b128 v[56:59], v85 offset:49152
	v_add_co_u32_e32 v114, vcc, s15, v88
	s_waitcnt lgkmcnt(3)
	v_mfma_f32_16x16x32_f16 v[44:47], v[44:47], v[14:17], v[52:55]
	v_addc_co_u32_e32 v115, vcc, 0, v89, vcc
	s_waitcnt lgkmcnt(2)
	v_mfma_f32_16x16x32_f16 v[44:47], v[72:75], v[10:13], v[44:47]
	ds_read_b128 v[52:55], v60 offset:49152
	v_add_u32_e32 v60, v133, v147
	v_lshlrev_b32_e32 v72, 8, v60
	v_lshlrev_b32_e32 v60, 2, v60
	v_mfma_f32_16x16x32_f16 v[44:47], v[68:71], v[6:9], v[44:47]
	v_and_b32_e32 v60, 12, v60
	v_or_b32_e32 v68, v60, v61
	v_bitop3_b32 v60, v236, v60, v61 bitop3:0x1e
	v_lshl_or_b32 v69, v60, 4, v72
	s_waitcnt lgkmcnt(2)
	v_mfma_f32_16x16x32_f16 v[44:47], v[76:79], v[2:5], v[44:47]
	ds_read_b128 v[60:63], v69
	v_bitop3_b32 v70, v236, v68, 4 bitop3:0x36
	v_lshl_or_b32 v70, v70, 4, v72
	s_waitcnt lgkmcnt(2)
	v_mfma_f32_16x16x32_f16 v[44:47], v[56:59], v[40:43], v[44:47]
	ds_read_b128 v[56:59], v70
	v_bitop3_b32 v71, v236, v68, 8 bitop3:0x36
	v_lshl_or_b32 v71, v71, 4, v72
	s_waitcnt lgkmcnt(1)
	v_mfma_f32_16x16x32_f16 v[22:25], v[60:63], v[22:25], 0
	v_bitop3_b32 v60, v236, v68, 12 bitop3:0x36
	v_lshl_or_b32 v68, v60, 4, v72
	ds_read_b32 v210, v209
	v_mfma_f32_16x16x32_f16 v[126:129], v[52:55], v[106:109], v[44:47]
	s_nop 2
	ds_read_b128 v[44:47], v71
	ds_read_b128 v[52:55], v69 offset:49152
	ds_read_b128 v[60:63], v70 offset:49152
	s_waitcnt lgkmcnt(4)
	v_mfma_f32_16x16x32_f16 v[18:21], v[56:59], v[18:21], v[22:25]
	ds_read_b128 v[56:59], v71 offset:49152
	s_nop 1
	ds_read_b128 v[22:25], v68
	s_waitcnt lgkmcnt(4)
	v_mfma_f32_16x16x32_f16 v[14:17], v[44:47], v[14:17], v[18:21]
	v_add_co_u32_e32 v44, vcc, s5, v88
	s_movk_i32 s5, 0x3000
	s_nop 0
	ds_read_b128 v[18:21], v68 offset:49152
	s_waitcnt lgkmcnt(1)
	v_mfma_f32_16x16x32_f16 v[10:13], v[22:25], v[10:13], v[14:17]
	v_addc_co_u32_e32 v45, vcc, 0, v89, vcc
	global_load_dwordx4 v[84:87], v[114:115], off offset:1024
	global_load_dwordx4 v[80:83], v[114:115], off offset:2048
	global_load_dwordx4 v[92:95], v[44:45], off offset:-4096
	global_load_dwordx4 v[76:79], v[44:45], off
	v_mfma_f32_16x16x32_f16 v[6:9], v[52:55], v[6:9], v[10:13]
	global_load_dwordx4 v[72:75], v[44:45], off offset:1024
	global_load_dwordx4 v[68:71], v[44:45], off offset:2048
	global_load_dwordx4 v[52:55], v[44:45], off offset:3072
	v_mov_b32_e32 v13, 0xff61b1e6
	v_mfma_f32_16x16x32_f16 v[2:5], v[60:63], v[2:5], v[6:9]
	s_nop 2
	v_add_co_u32_e32 v6, vcc, s5, v88
	v_mfma_f32_16x16x32_f16 v[2:5], v[56:59], v[40:43], v[2:5]
	s_nop 0
	v_addc_co_u32_e32 v7, vcc, 0, v89, vcc
	global_load_dwordx4 v[88:91], v[114:115], off offset:3072
	global_load_dwordx4 v[60:63], v[6:7], off
	global_load_dwordx4 v[56:59], v[6:7], off offset:1024
	global_load_dwordx4 v[44:47], v[6:7], off offset:2048
	global_load_dwordx4 v[40:43], v[6:7], off offset:3072
	s_waitcnt lgkmcnt(0)
	v_mfma_f32_16x16x32_f16 v[16:19], v[18:21], v[106:109], v[2:5]
	s_mov_b32 s5, 0xff61b1e6
	s_nop 0
	v_or_b32_e32 v3, s14, v146
	v_mov_b32_e32 v4, 0x7df
	v_med3_u32 v3, v3, 32, v4
	v_or_b32_e32 v4, v97, v102
	v_sub_u32_e32 v3, v4, v3
	v_add_f32_e32 v2, s4, v210
	v_add_u32_e32 v3, 32, v3
	v_mad_u32_u24 v4, v103, 48, v3
	s_movk_i32 s4, 0x41
	v_add_f32_e32 v5, v2, v110
	v_mul_f32_e32 v5, 0x3db8aa3b, v5
	v_cmp_gt_u32_e32 vcc, s4, v4
	v_add_u32_e32 v6, 1, v4
	v_add_f32_e32 v7, v2, v111
	v_cndmask_b32_e32 v5, v13, v5, vcc
	v_mul_f32_e32 v7, 0x3db8aa3b, v7
	v_cmp_gt_u32_e32 vcc, s4, v6
	v_add_u32_e32 v8, 2, v4
	v_add_f32_e32 v9, v2, v112
	v_cndmask_b32_e32 v6, v13, v7, vcc
	v_mul_f32_e32 v9, 0x3db8aa3b, v9
	v_cmp_gt_u32_e32 vcc, s4, v8
	v_add_u32_e32 v4, 3, v4
	v_max3_f32 v7, v5, s5, v6
	v_cndmask_b32_e32 v8, v13, v9, vcc
	v_add_f32_e32 v9, v2, v113
	v_mul_f32_e32 v9, 0x3db8aa3b, v9
	v_cmp_gt_u32_e32 vcc, s4, v4
	v_add_u32_e32 v11, v3, v132
	v_add_f32_e32 v12, v2, v127
	v_cndmask_b32_e32 v10, v13, v9, vcc
	v_max3_f32 v4, v7, v8, v10
	v_add_f32_e32 v7, v2, v126
	v_mul_f32_e32 v7, 0x3db8aa3b, v7
	v_cmp_gt_u32_e32 vcc, s4, v11
	v_add_u32_e32 v9, 1, v11
	v_mul_f32_e32 v12, 0x3db8aa3b, v12
	v_cndmask_b32_e32 v7, v13, v7, vcc
	v_cmp_gt_u32_e32 vcc, s4, v9
	v_add_f32_e32 v14, v2, v128
	v_mul_f32_e32 v14, 0x3db8aa3b, v14
	v_cndmask_b32_e32 v9, v13, v12, vcc
	v_add_u32_e32 v12, 2, v11
	v_cmp_gt_u32_e32 vcc, s4, v12
	v_add_u32_e32 v11, 3, v11
	v_add_u32_e32 v3, v3, v133
	v_cndmask_b32_e32 v12, v13, v14, vcc
	v_add_f32_e32 v14, v2, v129
	v_mul_f32_e32 v14, 0x3db8aa3b, v14
	v_cmp_gt_u32_e32 vcc, s4, v11
	v_add_f32_e32 v11, v2, v16
	v_mul_f32_e32 v11, 0x3db8aa3b, v11
	v_cndmask_b32_e32 v15, v13, v14, vcc
	v_cmp_gt_u32_e32 vcc, s4, v3
	v_add_u32_e32 v14, 1, v3
	v_add_f32_e32 v16, v2, v17
	v_cndmask_b32_e32 v11, v13, v11, vcc
	v_mul_f32_e32 v16, 0x3db8aa3b, v16
	v_cmp_gt_u32_e32 vcc, s4, v14
	v_add_f32_e32 v17, v2, v18
	v_max3_f32 v4, v4, v7, v9
	v_cndmask_b32_e32 v14, v13, v16, vcc
	v_add_u32_e32 v16, 2, v3
	v_mul_f32_e32 v17, 0x3db8aa3b, v17
	v_cmp_gt_u32_e32 vcc, s4, v16
	v_add_u32_e32 v3, 3, v3
	v_add_f32_e32 v2, v2, v19
	v_max3_f32 v4, v4, v12, v15
	v_cndmask_b32_e32 v16, v13, v17, vcc
	v_mul_f32_e32 v2, 0x3db8aa3b, v2
	v_cmp_gt_u32_e32 vcc, s4, v3
	v_max3_f32 v4, v4, v11, v14
	v_lshlrev_b32_e32 v126, 5, v99
	v_cndmask_b32_e32 v17, v13, v2, vcc
	v_max3_f32 v2, v4, v16, v17
	v_mov_b32_e32 v3, v2
	v_lshlrev_b32_e32 v127, 2, v119
	v_lshrrev_b32_e32 v4, 7, v0
	v_cmp_gt_u32_e32 vcc, 16, v98
	v_permlane16_swap_b32_e32 v3, v2
	v_max_f32_e32 v2, v2, v3
	v_mov_b32_e32 v3, v2
	s_nop 1
	v_permlane32_swap_b32_e32 v3, v2
	v_max_f32_e32 v13, v2, v3
	v_and_b32_e32 v2, 0x180, v0
	v_or_b32_e32 v2, 0x23400, v2
	v_lshlrev_b32_e32 v3, 2, v100
	s_and_saveexec_b64 s[4:5], vcc
	v_lshlrev_b32_e32 v18, 6, v103
	v_add3_u32 v18, v2, v18, v3
	ds_write_b32 v18, v13
	s_or_b64 exec, exec, s[4:5]
	v_lshlrev_b32_e32 v18, 4, v103
	v_bitop3_b32 v19, v18, 16, v100 bitop3:0x36
	v_lshl_add_u32 v2, v19, 2, v2
	s_waitcnt lgkmcnt(0)
	s_barrier
	ds_read_b32 v19, v2
	v_max_f32_e32 v13, v13, v13
	v_mul_u32_u24_e32 v20, 0xd00, v4
	s_load_dwordx2 s[0:1], s[0:1], 0x30
	v_or_b32_e32 v2, 1, v124
	s_waitcnt lgkmcnt(0)
	v_max_f32_e32 v19, v19, v19
	v_max_f32_e32 v19, v13, v19
	v_sub_f32_e32 v5, v5, v19
	v_exp_f32_e32 v5, v5
	v_sub_f32_e32 v6, v6, v19
	v_exp_f32_e32 v6, v6
	v_sub_f32_e32 v8, v8, v19
	v_mul_u32_u24_e32 v13, 0xd0, v100
	v_exp_f32_e32 v8, v8
	v_sub_f32_e32 v10, v10, v19
	v_add3_u32 v20, v13, v20, v29
	v_exp_f32_e32 v10, v10
	v_or_b32_e32 v22, 0x20000, v20
	v_add_f32_e32 v20, 0, v5
	v_add_f32_e32 v20, v20, v6
	v_add_f32_e32 v20, v20, v8
	v_add_f32_e32 v23, v20, v10
	v_cvt_pk_f16_f32 v21, v8, v10
	v_cvt_pk_f16_f32 v20, v5, v6
	v_mad_u32_u24 v5, v103, s16, v22
	ds_write_b64 v5, v[20:21]
	v_sub_f32_e32 v5, v7, v19
	v_exp_f32_e32 v5, v5
	v_sub_f32_e32 v6, v9, v19
	v_exp_f32_e32 v6, v6
	v_sub_f32_e32 v7, v12, v19
	v_exp_f32_e32 v7, v7
	v_sub_f32_e32 v8, v15, v19
	v_exp_f32_e32 v8, v8
	v_sub_f32_e32 v10, v11, v19
	v_add_f32_e32 v9, v23, v5
	v_exp_f32_e32 v10, v10
	v_sub_f32_e32 v11, v14, v19
	v_add_f32_e32 v9, v9, v6
	v_exp_f32_e32 v11, v11
	v_sub_f32_e32 v12, v16, v19
	v_add_f32_e32 v9, v9, v7
	v_exp_f32_e32 v12, v12
	v_sub_f32_e32 v14, v17, v19
	v_add_f32_e32 v9, v9, v8
	v_exp_f32_e32 v14, v14
	v_add_f32_e32 v9, v9, v10
	v_add_f32_e32 v9, v9, v11
	v_add_f32_e32 v9, v9, v12
	v_add_f32_e32 v9, v9, v14
	v_mov_b32_e32 v15, v9
	v_cvt_pk_f16_f32 v7, v7, v8
	v_cvt_pk_f16_f32 v6, v5, v6
	v_lshl_add_u32 v5, v104, 5, v22
	ds_write_b64 v5, v[6:7]
	v_permlane16_swap_b32_e32 v15, v9
	v_add_f32_e32 v5, v9, v15
	v_mov_b32_e32 v6, v5
	s_movk_i32 s7, 0xd00
	s_mov_b32 s6, 0x20000
	v_cvt_pk_f16_f32 v9, v12, v14
	v_cvt_pk_f16_f32 v8, v10, v11
	v_lshl_add_u32 v7, v105, 5, v22
	ds_write_b64 v7, v[8:9]
	v_permlane32_swap_b32_e32 v6, v5
	s_and_saveexec_b64 s[4:5], vcc
	s_cbranch_execz .LBB1_4
	v_lshlrev_b32_e32 v4, 5, v4
	v_or_b32_e32 v7, v18, v100
	v_lshlrev_b32_e32 v4, 2, v4
	v_lshlrev_b32_e32 v7, 2, v7
	s_mov_b32 s8, 0x23600
	v_add3_u32 v4, v7, v4, s8
	v_add_f32_e32 v5, v5, v6
	ds_write_b32 v4, v5
